# static s_setprio 1 for wave 0 only (it owns the serial gate recursion) across the P4 mLSTM phase, reset at phase end
# speedup vs baseline: 1.0010x; 1.0010x over previous
.LBB0_609:
	s_or_b64 exec, exec, s[0:1]
	v_mov_b32_e32 v108, v0
	s_waitcnt lgkmcnt(0)
	v_mov_b32_e32 v1, s76
	v_mov_b32_e32 v2, s77
	s_barrier
	s_add_i32 s0, 0, 0x25d38
	v_readfirstlane_b32 s1, v2
	v_mov_b32_e32 v2, s78
	v_mov_b32_e32 v4, s74
	v_mov_b32_e32 v5, s75
	v_mov_b32_e32 v2, s0
	ds_read_b64 v[2:3], v2
	v_readfirstlane_b32 s46, v4
	v_readfirstlane_b32 s2, v1
	v_readfirstlane_b32 s39, v5
	s_mov_b32 s35, 0
	s_waitcnt lgkmcnt(0)
	v_readfirstlane_b32 s4, v2
	v_readfirstlane_b32 s5, v3
	s_cmpk_gt_i32 s46, 0xff
	v_writelane_b32 v243, s4, 14
	v_readfirstlane_b32 s3, v108
	s_nop 0
	v_writelane_b32 v243, s5, 15
	s_cbranch_scc1 .LBB0_825
	v_readfirstlane_b32 s98, v0
	s_nop 3
	s_cmp_gt_u32 s98, 63
	s_cbranch_scc1 .Lp4w0prio0
	s_setprio 1

.LBB0_2009:
	s_add_i32 s3, 0, 0x25d38
	v_mov_b32_e32 v1, s3
	ds_read_b64 v[2:3], v1
	v_readfirstlane_b32 s3, v104
	s_cmpk_gt_i32 s54, 0xff
	s_waitcnt lgkmcnt(0)
	v_readfirstlane_b32 s4, v2
	v_readfirstlane_b32 s5, v3
	s_nop 0
	v_writelane_b32 v243, s4, 25
	s_nop 1
	v_writelane_b32 v243, s5, 26
	s_cbranch_scc1 .LBB0_2237
	v_readfirstlane_b32 s98, v0
	s_nop 3
	s_cmp_gt_u32 s98, 63
	s_cbranch_scc1 .Lp4w0prio1
	s_setprio 1

.LBB0_3626:
	s_or_b64 exec, exec, s[0:1]
	s_load_dwordx2 s[0:1], s[80:81], 0xf0
	v_mov_b32_e32 v104, v0
	s_waitcnt lgkmcnt(0)
	s_barrier
	v_mov_b32_e32 v1, s0
	v_mov_b32_e32 v2, s1
	s_add_i32 s0, 0, 0x25d38
	v_readfirstlane_b32 s2, v2
	v_mov_b32_e32 v2, s79
	v_mov_b32_e32 v4, s77
	v_mov_b32_e32 v5, s78
	v_mov_b32_e32 v2, s0
	ds_read_b64 v[2:3], v2
	v_readfirstlane_b32 s52, v4
	v_readfirstlane_b32 s3, v1
	v_readfirstlane_b32 s53, v5
	s_mov_b32 s35, 0
	s_waitcnt lgkmcnt(0)
	v_readfirstlane_b32 s0, v2
	v_readfirstlane_b32 s1, v3
	s_cmpk_gt_i32 s52, 0xff
	v_writelane_b32 v243, s0, 27
	v_readfirstlane_b32 s10, v104
	s_nop 0
	v_writelane_b32 v243, s1, 28
	s_cbranch_scc1 .LBB0_3854
	v_readfirstlane_b32 s98, v0
	s_nop 3
	s_cmp_gt_u32 s98, 63
	s_cbranch_scc1 .Lp4w0prio2
	s_setprio 1

.LBB0_4989:
	s_or_b64 exec, exec, s[0:1]
	v_readlane_b32 s0, v243, 8
	v_readlane_b32 s1, v243, 9
	v_mov_b32_e32 v104, v0
	s_waitcnt lgkmcnt(0)
	v_mov_b32_e32 v1, s0
	v_mov_b32_e32 v2, s1
	s_barrier
	s_add_i32 s0, 0, 0x25d38
	v_readfirstlane_b32 s12, v2
	v_mov_b32_e32 v2, s79
	v_mov_b32_e32 v4, s77
	v_mov_b32_e32 v5, s78
	v_mov_b32_e32 v2, s0
	ds_read_b64 v[2:3], v2
	v_readfirstlane_b32 s50, v4
	v_readfirstlane_b32 s13, v1
	v_readfirstlane_b32 s44, v5
	s_mov_b32 s31, 0
	s_waitcnt lgkmcnt(0)
	v_readfirstlane_b32 s0, v2
	v_readfirstlane_b32 s1, v3
	s_cmpk_gt_i32 s50, 0xff
	v_writelane_b32 v243, s0, 27
	v_readfirstlane_b32 s8, v104
	s_nop 0
	v_writelane_b32 v243, s1, 28
	s_cbranch_scc1 .LBB0_5217
	v_readfirstlane_b32 s98, v0
	s_nop 3
	s_cmp_gt_u32 s98, 63
	s_cbranch_scc1 .Lp4w0prio3
	s_setprio 1
